# baseline (speedup 1.0000x reference)
.LBB2_5:
	s_waitcnt lgkmcnt(14)
	v_mfma_f32_32x32x16_f16 v[2:17], v[158:161], v[126:129], v[2:17]
	v_exp_f32_e32 v66, v66
	v_exp_f32_e32 v67, v67
	v_exp_f32_e32 v68, v68
	v_exp_f32_e32 v69, v69
	s_waitcnt lgkmcnt(12)
	v_mfma_f32_32x32x16_f16 v[18:33], v[158:161], v[122:125], v[18:33]
	v_exp_f32_e32 v70, v70
	v_exp_f32_e32 v71, v71
	v_exp_f32_e32 v72, v72
	v_exp_f32_e32 v73, v73
	v_add_u32_e32 v90, s43, v211
	ds_read_b128 v[82:85], v90
	ds_read_b128 v[170:173], v90 offset:4096
	s_waitcnt lgkmcnt(12)
	v_mfma_f32_32x32x16_f16 v[2:17], v[150:153], v[118:121], v[2:17]
	v_exp_f32_e32 v74, v74
	v_exp_f32_e32 v75, v75
	v_exp_f32_e32 v76, v76
	v_exp_f32_e32 v77, v77
	v_add_u32_e32 v90, s43, v210
	ds_read_b128 v[166:169], v90
	ds_read_b128 v[162:165], v90 offset:4096
	s_waitcnt lgkmcnt(12)
	v_mfma_f32_32x32x16_f16 v[18:33], v[150:153], v[114:117], v[18:33]
	v_exp_f32_e32 v78, v78
	v_exp_f32_e32 v79, v79
	v_exp_f32_e32 v80, v80
	v_exp_f32_e32 v81, v81
	v_add_u32_e32 v90, s43, v209
	ds_read_b128 v[126:129], v90
	ds_read_b128 v[122:125], v90 offset:4096
	s_waitcnt lgkmcnt(12)
	v_mfma_f32_32x32x16_f16 v[2:17], v[142:145], v[106:109], v[2:17]
	v_exp_f32_e32 v50, v50
	v_exp_f32_e32 v51, v51
	v_exp_f32_e32 v52, v52
	v_exp_f32_e32 v53, v53
	v_add_u32_e32 v90, s43, v208
	ds_read_b128 v[118:121], v90
	ds_read_b128 v[114:117], v90 offset:4096
	s_waitcnt lgkmcnt(12)
	v_mfma_f32_32x32x16_f16 v[18:33], v[142:145], v[102:105], v[18:33]
	v_exp_f32_e32 v54, v54
	v_exp_f32_e32 v55, v55
	v_exp_f32_e32 v56, v56
	v_exp_f32_e32 v57, v57
	s_waitcnt lgkmcnt(10)
	v_mfma_f32_32x32x16_f16 v[2:17], v[130:133], v[98:101], v[2:17]
	v_exp_f32_e32 v58, v58
	v_exp_f32_e32 v59, v59
	v_exp_f32_e32 v60, v60
	v_exp_f32_e32 v61, v61
	s_waitcnt lgkmcnt(8)
	v_mfma_f32_32x32x16_f16 v[18:33], v[130:133], v[86:89], v[18:33]
	v_exp_f32_e32 v62, v62
	v_exp_f32_e32 v63, v63
	v_exp_f32_e32 v64, v64
	v_exp_f32_e32 v65, v65
	s_add_i32 s44, s43, 0x2000
	s_cmpk_lg_i32 s43, 0x4000
	s_cselect_b32 s45, s44, 0
	s_add_i32 s40, s40, 2
	v_lshl_add_u64 v[188:189], v[188:189], 0, s[22:23]
	s_waitcnt vmcnt(2) lgkmcnt(0)
	s_barrier
	s_andn2_b64 vcc, exec, s[26:27]
	s_cbranch_vccnz .LBB2_7
	s_waitcnt lgkmcnt(0)
	v_add_u32_e32 v98, s38, v212
	ds_read_b128 v[86:89], v98 offset:49248
	ds_read_b128 v[90:93], v98 offset:49216
	ds_read_b128 v[94:97], v98 offset:49152
	ds_read_b128 v[98:101], v98 offset:49184
	s_waitcnt lgkmcnt(3)
	v_pk_mul_f32 v[16:17], v[16:17], v[88:89]
	v_pk_mul_f32 v[14:15], v[14:15], v[86:87]
	s_waitcnt lgkmcnt(2)
	v_pk_mul_f32 v[12:13], v[12:13], v[92:93]
	v_pk_mul_f32 v[10:11], v[10:11], v[90:91]
	s_waitcnt lgkmcnt(0)
	v_pk_mul_f32 v[8:9], v[8:9], v[100:101]
	v_pk_mul_f32 v[6:7], v[6:7], v[98:99]
	v_pk_mul_f32 v[4:5], v[4:5], v[96:97]
	v_pk_mul_f32 v[2:3], v[2:3], v[94:95]
	v_pk_mul_f32 v[32:33], v[32:33], v[88:89]
	v_pk_mul_f32 v[30:31], v[30:31], v[86:87]
	v_pk_mul_f32 v[28:29], v[28:29], v[92:93]
	v_pk_mul_f32 v[26:27], v[26:27], v[90:91]
	v_pk_mul_f32 v[24:25], v[24:25], v[100:101]
	v_pk_mul_f32 v[22:23], v[22:23], v[98:99]
	v_pk_mul_f32 v[20:21], v[20:21], v[96:97]
	v_pk_mul_f32 v[18:19], v[18:19], v[94:95]
.LBB2_7:
	s_cmp_lt_u32 s40, 25
	s_cbranch_scc1 .Lattn_rot_cont
	s_mov_b32 s26, s44
	s_mov_b32 s27, s45
	s_branch .LBB2_15
.Lattn_rot_cont:
	s_mov_b32 s26, s39
	s_mov_b32 s42, s43
	s_mov_b32 s39, s45
	s_branch .LBB2_1
